# hand-written double-buffered expert-weight converter (2 items of loads in flight per workgroup, 1 barrier per item) on 120 workgroups instead of 144, plus the spread expert counters
# speedup vs baseline: 1.0235x; 1.0235x over previous
.LBB0_226:
	s_cmp_lt_i32 s28, 3
	s_cselect_b64 s[0:1], -1, 0
	s_cmp_gt_i32 s29, 2
	s_cselect_b64 s[6:7], -1, 0
	s_and_b64 s[0:1], s[0:1], s[6:7]
	s_andn2_b64 vcc, exec, s[0:1]
	s_cbranch_vccnz .LBB0_398
	s_cmpk_lg_i32 s33, 0x100
	s_cselect_b32 s3, s33, 0x78
	s_sub_i32 s6, s33, s3
	s_cmp_lt_i32 s2, s6
	s_cselect_b64 s[0:1], -1, 0
	s_sub_i32 s30, s2, s6
	s_cmpk_gt_i32 s30, 0x2fff
	s_cselect_b64 s[6:7], -1, 0
	s_or_b64 s[0:1], s[0:1], s[6:7]
	v_lshrrev_b32_e32 v82, 5, v0
	v_lshlrev_b32_e32 v80, 4, v0
	v_lshrrev_b32_e32 v1, 7, v0
	v_lshrrev_b32_e32 v81, 3, v0
	s_and_b64 vcc, exec, s[0:1]
	s_cbranch_vccnz .LBB0_237
	v_readlane_b32 s6, v252, 0
	v_readlane_b32 s7, v252, 1
	v_readfirstlane_b32 s34, v0
	s_nop 4
	s_sub_u32 s6, s6, 0xe8
	s_subb_u32 s7, s7, 0
	s_load_dwordx2 s[8:9], s[6:7], 0xa8
	s_load_dwordx2 s[10:11], s[6:7], 0xb8
	s_lshr_b32 s34, s34, 6
	s_add_u32 s12, s26, 0x5800000
	s_addc_u32 s13, s27, 0
	s_add_u32 s14, s26, 0x25800000
	s_addc_u32 s15, s27, 0
	s_mov_b32 s35, 0xc3e00000
	v_mov_b32_e32 v160, 0x43e00000
	s_mov_b32 s31, 120
	s_sub_u32 s0, 0x2fff, s30
	s_mul_hi_u32 s41, s0, 0x2222223
	s_add_u32 s41, s41, 1
	v_and_b32_e32 v77, 63, v0
	v_and_b32_e32 v66, 31, v77
	v_lshlrev_b32_e32 v66, 4, v66
	v_lshrrev_b32_e32 v67, 5, v77
	v_lshl_add_u32 v68, v67, 13, v66
	v_lshl_add_u32 v69, v67, 9, v66
	s_lshr_b32 s0, s34, 1
	v_and_b32_e32 v78, 3, v77
	v_xor_b32_e32 v78, s0, v78
	v_and_b32_e32 v71, 4, v77
	v_or_b32_e32 v78, v78, v71
	v_lshlrev_b32_e32 v78, 4, v78
	s_and_b32 s0, s34, 1
	s_lshl_b32 s0, s0, 3
	v_lshl_or_b32 v71, v77, 9, s0
	v_or_b32_e32 v71, v71, v78
	v_xor_b32_e32 v72, 64, v71
	v_add_u32_e32 v73, 0x8000, v71
	v_add_u32_e32 v74, 0x8000, v72
	s_lshl_b32 s0, s34, 1
	v_add_u32_e32 v78, s0, v67
	v_xor_b32_e32 v78, v78, v77
	v_and_b32_e32 v78, 7, v78
	v_lshlrev_b32_e32 v78, 4, v78
	v_lshrrev_b32_e32 v75, 3, v77
	s_lshl_b32 s0, s34, 3
	v_add_u32_e32 v75, s0, v75
	v_and_b32_e32 v76, 7, v77
	v_lshlrev_b32_e32 v76, 4, v76
	v_lshl_add_u32 v76, v75, 11, v76
	v_lshl_add_u32 v75, v75, 7, v78
	s_waitcnt lgkmcnt(0)
	s_min_u32 s0, s30, 0x2fff
	s_add_u32 s30, s30, s31
	s_cmp_lt_u32 s0, 0x2000
	s_cbranch_scc0 .Lcv_w2_1
	s_lshr_b32 s1, s0, 8
	s_bfe_u32 s3, s0, 0x40004
	s_and_b32 s0, s0, 15
	s_lshl_b32 s6, s1, 25
	s_lshl_b32 s7, s3, 21
	s_add_u32 s6, s6, s7
	s_lshl_b32 s7, s34, 17
	s_add_u32 s6, s6, s7
	s_lshl_b32 s7, s0, 9
	s_add_u32 s6, s6, s7
	s_add_u32 s62, s8, s6
	s_addc_u32 s63, s9, 0
	s_lshl_b32 s6, s1, 23
	s_lshl_b32 s7, s0, 19
	s_add_u32 s6, s6, s7
	s_lshl_b32 s7, s3, 7
	s_add_u32 s6, s6, s7
	s_add_u32 s52, s12, s6
	s_addc_u32 s53, s13, 0
	s_mov_b32 s70, 0x4000
	s_mov_b32 s71, 0xe4000
	v_mov_b32_e32 v70, v68
	s_branch .Lcv_dec_done_1
.Lcv_w2_1:
	s_sub_u32 s0, s0, 0x2000
	s_lshr_b32 s1, s0, 7
	s_bfe_u32 s3, s0, 0x40003
	s_and_b32 s0, s0, 7
	s_lshl_b32 s6, s1, 24
	s_lshl_b32 s7, s3, 20
	s_add_u32 s6, s6, s7
	s_lshl_b32 s7, s34, 16
	s_add_u32 s6, s6, s7
	s_lshl_b32 s7, s0, 10
	s_add_u32 s6, s6, s7
	s_add_u32 s62, s10, s6
	s_addc_u32 s63, s11, 0
	s_lshl_b32 s6, s1, 22
	s_lshl_b32 s7, s0, 19
	s_add_u32 s6, s6, s7
	s_lshl_b32 s7, s3, 7
	s_add_u32 s6, s6, s7
	s_add_u32 s52, s14, s6
	s_addc_u32 s53, s15, 0
	s_mov_b32 s70, 0x2000
	s_mov_b32 s71, 0x72000
	v_mov_b32_e32 v70, v69
.Lcv_dec_done_1:
	global_load_dwordx4 v[2:5], v70, s[62:63] nt
	s_add_u32 s62, s62, s70
	s_addc_u32 s63, s63, 0
	global_load_dwordx4 v[6:9], v70, s[62:63] nt
	s_add_u32 s62, s62, s70
	s_addc_u32 s63, s63, 0
	global_load_dwordx4 v[10:13], v70, s[62:63] nt
	s_add_u32 s62, s62, s70
	s_addc_u32 s63, s63, 0
	global_load_dwordx4 v[14:17], v70, s[62:63] nt
	s_add_u32 s62, s62, s70
	s_addc_u32 s63, s63, 0
	global_load_dwordx4 v[18:21], v70, s[62:63] nt
	s_add_u32 s62, s62, s70
	s_addc_u32 s63, s63, 0
	global_load_dwordx4 v[22:25], v70, s[62:63] nt
	s_add_u32 s62, s62, s70
	s_addc_u32 s63, s63, 0
	global_load_dwordx4 v[26:29], v70, s[62:63] nt
	s_add_u32 s62, s62, s70
	s_addc_u32 s63, s63, 0
	global_load_dwordx4 v[30:33], v70, s[62:63] nt
	s_add_u32 s62, s62, s71
	s_addc_u32 s63, s63, 0
	global_load_dwordx4 v[34:37], v70, s[62:63] nt
	s_add_u32 s62, s62, s70
	s_addc_u32 s63, s63, 0
	global_load_dwordx4 v[38:41], v70, s[62:63] nt
	s_add_u32 s62, s62, s70
	s_addc_u32 s63, s63, 0
	global_load_dwordx4 v[42:45], v70, s[62:63] nt
	s_add_u32 s62, s62, s70
	s_addc_u32 s63, s63, 0
	global_load_dwordx4 v[46:49], v70, s[62:63] nt
	s_add_u32 s62, s62, s70
	s_addc_u32 s63, s63, 0
	global_load_dwordx4 v[50:53], v70, s[62:63] nt
	s_add_u32 s62, s62, s70
	s_addc_u32 s63, s63, 0
	global_load_dwordx4 v[54:57], v70, s[62:63] nt
	s_add_u32 s62, s62, s70
	s_addc_u32 s63, s63, 0
	global_load_dwordx4 v[58:61], v70, s[62:63] nt
	s_add_u32 s62, s62, s70
	s_addc_u32 s63, s63, 0
	global_load_dwordx4 v[62:65], v70, s[62:63] nt
	s_min_u32 s0, s30, 0x2fff
	s_add_u32 s30, s30, s31
	s_cmp_lt_u32 s0, 0x2000
	s_cbranch_scc0 .Lcv_w2_2
	s_lshr_b32 s1, s0, 8
	s_bfe_u32 s3, s0, 0x40004
	s_and_b32 s0, s0, 15
	s_lshl_b32 s6, s1, 25
	s_lshl_b32 s7, s3, 21
	s_add_u32 s6, s6, s7
	s_lshl_b32 s7, s34, 17
	s_add_u32 s6, s6, s7
	s_lshl_b32 s7, s0, 9
	s_add_u32 s6, s6, s7
	s_add_u32 s62, s8, s6
	s_addc_u32 s63, s9, 0
	s_lshl_b32 s6, s1, 23
	s_lshl_b32 s7, s0, 19
	s_add_u32 s6, s6, s7
	s_lshl_b32 s7, s3, 7
	s_add_u32 s6, s6, s7
	s_add_u32 s58, s12, s6
	s_addc_u32 s59, s13, 0
	s_mov_b32 s70, 0x4000
	s_mov_b32 s71, 0xe4000
	v_mov_b32_e32 v70, v68
	s_branch .Lcv_dec_done_2
.Lcv_w2_2:
	s_sub_u32 s0, s0, 0x2000
	s_lshr_b32 s1, s0, 7
	s_bfe_u32 s3, s0, 0x40003
	s_and_b32 s0, s0, 7
	s_lshl_b32 s6, s1, 24
	s_lshl_b32 s7, s3, 20
	s_add_u32 s6, s6, s7
	s_lshl_b32 s7, s34, 16
	s_add_u32 s6, s6, s7
	s_lshl_b32 s7, s0, 10
	s_add_u32 s6, s6, s7
	s_add_u32 s62, s10, s6
	s_addc_u32 s63, s11, 0
	s_lshl_b32 s6, s1, 22
	s_lshl_b32 s7, s0, 19
	s_add_u32 s6, s6, s7
	s_lshl_b32 s7, s3, 7
	s_add_u32 s6, s6, s7
	s_add_u32 s58, s14, s6
	s_addc_u32 s59, s15, 0
	s_mov_b32 s70, 0x2000
	s_mov_b32 s71, 0x72000
	v_mov_b32_e32 v70, v69
.Lcv_dec_done_2:
	global_load_dwordx4 v[84:87], v70, s[62:63] nt
	s_add_u32 s62, s62, s70
	s_addc_u32 s63, s63, 0
	global_load_dwordx4 v[88:91], v70, s[62:63] nt
	s_add_u32 s62, s62, s70
	s_addc_u32 s63, s63, 0
	global_load_dwordx4 v[92:95], v70, s[62:63] nt
	s_add_u32 s62, s62, s70
	s_addc_u32 s63, s63, 0
	global_load_dwordx4 v[96:99], v70, s[62:63] nt
	s_add_u32 s62, s62, s70
	s_addc_u32 s63, s63, 0
	global_load_dwordx4 v[100:103], v70, s[62:63] nt
	s_add_u32 s62, s62, s70
	s_addc_u32 s63, s63, 0
	global_load_dwordx4 v[104:107], v70, s[62:63] nt
	s_add_u32 s62, s62, s70
	s_addc_u32 s63, s63, 0
	global_load_dwordx4 v[108:111], v70, s[62:63] nt
	s_add_u32 s62, s62, s70
	s_addc_u32 s63, s63, 0
	global_load_dwordx4 v[112:115], v70, s[62:63] nt
	s_add_u32 s62, s62, s71
	s_addc_u32 s63, s63, 0
	global_load_dwordx4 v[116:119], v70, s[62:63] nt
	s_add_u32 s62, s62, s70
	s_addc_u32 s63, s63, 0
	global_load_dwordx4 v[120:123], v70, s[62:63] nt
	s_add_u32 s62, s62, s70
	s_addc_u32 s63, s63, 0
	global_load_dwordx4 v[124:127], v70, s[62:63] nt
	s_add_u32 s62, s62, s70
	s_addc_u32 s63, s63, 0
	global_load_dwordx4 v[128:131], v70, s[62:63] nt
	s_add_u32 s62, s62, s70
	s_addc_u32 s63, s63, 0
	global_load_dwordx4 v[132:135], v70, s[62:63] nt
	s_add_u32 s62, s62, s70
	s_addc_u32 s63, s63, 0
	global_load_dwordx4 v[136:139], v70, s[62:63] nt
	s_add_u32 s62, s62, s70
	s_addc_u32 s63, s63, 0
	global_load_dwordx4 v[140:143], v70, s[62:63] nt
	s_add_u32 s62, s62, s70
	s_addc_u32 s63, s63, 0
	global_load_dwordx4 v[144:147], v70, s[62:63] nt
	s_waitcnt vmcnt(16)
	s_branch .Lcv_convA
.Lcv_loopA:
	s_waitcnt vmcnt(20)
.Lcv_convA:
	v_mul_f32_e32 v156, 0x44000000, v2
	v_mul_f32_e32 v157, 0x44000000, v6
	v_med3_f32 v156, v156, s35, v160
	v_med3_f32 v157, v157, s35, v160
	v_cvt_pk_fp8_f32 v148, v156, v157
	v_mul_f32_e32 v158, 0x44000000, v10
	v_mul_f32_e32 v159, 0x44000000, v14
	v_med3_f32 v158, v158, s35, v160
	v_med3_f32 v159, v159, s35, v160
	v_cvt_pk_fp8_f32 v148, v158, v159 op_sel:[0,0,1]
	v_mul_f32_e32 v156, 0x44000000, v18
	v_mul_f32_e32 v157, 0x44000000, v22
	v_med3_f32 v156, v156, s35, v160
	v_med3_f32 v157, v157, s35, v160
	v_cvt_pk_fp8_f32 v149, v156, v157
	v_mul_f32_e32 v158, 0x44000000, v26
	v_mul_f32_e32 v159, 0x44000000, v30
	v_med3_f32 v158, v158, s35, v160
	v_med3_f32 v159, v159, s35, v160
	v_cvt_pk_fp8_f32 v149, v158, v159 op_sel:[0,0,1]
	v_mul_f32_e32 v156, 0x44000000, v3
	v_mul_f32_e32 v157, 0x44000000, v7
	v_med3_f32 v156, v156, s35, v160
	v_med3_f32 v157, v157, s35, v160
	v_cvt_pk_fp8_f32 v150, v156, v157
	v_mul_f32_e32 v158, 0x44000000, v11
	v_mul_f32_e32 v159, 0x44000000, v15
	v_med3_f32 v158, v158, s35, v160
	v_med3_f32 v159, v159, s35, v160
	v_cvt_pk_fp8_f32 v150, v158, v159 op_sel:[0,0,1]
	v_mul_f32_e32 v156, 0x44000000, v19
	v_mul_f32_e32 v157, 0x44000000, v23
	v_med3_f32 v156, v156, s35, v160
	v_med3_f32 v157, v157, s35, v160
	v_cvt_pk_fp8_f32 v151, v156, v157
	v_mul_f32_e32 v158, 0x44000000, v27
	v_mul_f32_e32 v159, 0x44000000, v31
	v_med3_f32 v158, v158, s35, v160
	v_med3_f32 v159, v159, s35, v160
	v_cvt_pk_fp8_f32 v151, v158, v159 op_sel:[0,0,1]
	v_mul_f32_e32 v156, 0x44000000, v4
	v_mul_f32_e32 v157, 0x44000000, v8
	v_med3_f32 v156, v156, s35, v160
	v_med3_f32 v157, v157, s35, v160
	v_cvt_pk_fp8_f32 v152, v156, v157
	v_mul_f32_e32 v158, 0x44000000, v12
	v_mul_f32_e32 v159, 0x44000000, v16
	v_med3_f32 v158, v158, s35, v160
	v_med3_f32 v159, v159, s35, v160
	v_cvt_pk_fp8_f32 v152, v158, v159 op_sel:[0,0,1]
	ds_write2_b64 v71, v[148:149], v[150:151] offset0:0 offset1:16
	v_mul_f32_e32 v156, 0x44000000, v20
	v_mul_f32_e32 v157, 0x44000000, v24
	v_med3_f32 v156, v156, s35, v160
	v_med3_f32 v157, v157, s35, v160
	v_cvt_pk_fp8_f32 v153, v156, v157
	v_mul_f32_e32 v158, 0x44000000, v28
	v_mul_f32_e32 v159, 0x44000000, v32
	v_med3_f32 v158, v158, s35, v160
	v_med3_f32 v159, v159, s35, v160
	v_cvt_pk_fp8_f32 v153, v158, v159 op_sel:[0,0,1]
	v_mul_f32_e32 v156, 0x44000000, v5
	v_mul_f32_e32 v157, 0x44000000, v9
	v_med3_f32 v156, v156, s35, v160
	v_med3_f32 v157, v157, s35, v160
	v_cvt_pk_fp8_f32 v154, v156, v157
	v_mul_f32_e32 v158, 0x44000000, v13
	v_mul_f32_e32 v159, 0x44000000, v17
	v_med3_f32 v158, v158, s35, v160
	v_med3_f32 v159, v159, s35, v160
	v_cvt_pk_fp8_f32 v154, v158, v159 op_sel:[0,0,1]
	v_mul_f32_e32 v156, 0x44000000, v21
	v_mul_f32_e32 v157, 0x44000000, v25
	v_med3_f32 v156, v156, s35, v160
	v_med3_f32 v157, v157, s35, v160
	v_cvt_pk_fp8_f32 v155, v156, v157
	v_mul_f32_e32 v158, 0x44000000, v29
	v_mul_f32_e32 v159, 0x44000000, v33
	v_med3_f32 v158, v158, s35, v160
	v_med3_f32 v159, v159, s35, v160
	v_cvt_pk_fp8_f32 v155, v158, v159 op_sel:[0,0,1]
	v_mul_f32_e32 v156, 0x44000000, v34
	v_mul_f32_e32 v157, 0x44000000, v38
	v_med3_f32 v156, v156, s35, v160
	v_med3_f32 v157, v157, s35, v160
	v_cvt_pk_fp8_f32 v148, v156, v157
	v_mul_f32_e32 v158, 0x44000000, v42
	v_mul_f32_e32 v159, 0x44000000, v46
	v_med3_f32 v158, v158, s35, v160
	v_med3_f32 v159, v159, s35, v160
	v_cvt_pk_fp8_f32 v148, v158, v159 op_sel:[0,0,1]
	ds_write2_b64 v71, v[152:153], v[154:155] offset0:32 offset1:48
	v_mul_f32_e32 v156, 0x44000000, v50
	v_mul_f32_e32 v157, 0x44000000, v54
	v_med3_f32 v156, v156, s35, v160
	v_med3_f32 v157, v157, s35, v160
	v_cvt_pk_fp8_f32 v149, v156, v157
	v_mul_f32_e32 v158, 0x44000000, v58
	v_mul_f32_e32 v159, 0x44000000, v62
	v_med3_f32 v158, v158, s35, v160
	v_med3_f32 v159, v159, s35, v160
	v_cvt_pk_fp8_f32 v149, v158, v159 op_sel:[0,0,1]
	v_mul_f32_e32 v156, 0x44000000, v35
	v_mul_f32_e32 v157, 0x44000000, v39
	v_med3_f32 v156, v156, s35, v160
	v_med3_f32 v157, v157, s35, v160
	v_cvt_pk_fp8_f32 v150, v156, v157
	v_mul_f32_e32 v158, 0x44000000, v43
	v_mul_f32_e32 v159, 0x44000000, v47
	v_med3_f32 v158, v158, s35, v160
	v_med3_f32 v159, v159, s35, v160
	v_cvt_pk_fp8_f32 v150, v158, v159 op_sel:[0,0,1]
	v_mul_f32_e32 v156, 0x44000000, v51
	v_mul_f32_e32 v157, 0x44000000, v55
	v_med3_f32 v156, v156, s35, v160
	v_med3_f32 v157, v157, s35, v160
	v_cvt_pk_fp8_f32 v151, v156, v157
	v_mul_f32_e32 v158, 0x44000000, v59
	v_mul_f32_e32 v159, 0x44000000, v63
	v_med3_f32 v158, v158, s35, v160
	v_med3_f32 v159, v159, s35, v160
	v_cvt_pk_fp8_f32 v151, v158, v159 op_sel:[0,0,1]
	v_mul_f32_e32 v156, 0x44000000, v36
	v_mul_f32_e32 v157, 0x44000000, v40
	v_med3_f32 v156, v156, s35, v160
	v_med3_f32 v157, v157, s35, v160
	v_cvt_pk_fp8_f32 v152, v156, v157
	v_mul_f32_e32 v158, 0x44000000, v44
	v_mul_f32_e32 v159, 0x44000000, v48
	v_med3_f32 v158, v158, s35, v160
	v_med3_f32 v159, v159, s35, v160
	v_cvt_pk_fp8_f32 v152, v158, v159 op_sel:[0,0,1]
	ds_write2_b64 v72, v[148:149], v[150:151] offset0:0 offset1:16
	v_mul_f32_e32 v156, 0x44000000, v52
	v_mul_f32_e32 v157, 0x44000000, v56
	v_med3_f32 v156, v156, s35, v160
	v_med3_f32 v157, v157, s35, v160
	v_cvt_pk_fp8_f32 v153, v156, v157
	v_mul_f32_e32 v158, 0x44000000, v60
	v_mul_f32_e32 v159, 0x44000000, v64
	v_med3_f32 v158, v158, s35, v160
	v_med3_f32 v159, v159, s35, v160
	v_cvt_pk_fp8_f32 v153, v158, v159 op_sel:[0,0,1]
	v_mul_f32_e32 v156, 0x44000000, v37
	v_mul_f32_e32 v157, 0x44000000, v41
	v_med3_f32 v156, v156, s35, v160
	v_med3_f32 v157, v157, s35, v160
	v_cvt_pk_fp8_f32 v154, v156, v157
	v_mul_f32_e32 v158, 0x44000000, v45
	v_mul_f32_e32 v159, 0x44000000, v49
	v_med3_f32 v158, v158, s35, v160
	v_med3_f32 v159, v159, s35, v160
	v_cvt_pk_fp8_f32 v154, v158, v159 op_sel:[0,0,1]
	v_mul_f32_e32 v156, 0x44000000, v53
	v_mul_f32_e32 v157, 0x44000000, v57
	v_med3_f32 v156, v156, s35, v160
	v_med3_f32 v157, v157, s35, v160
	v_cvt_pk_fp8_f32 v155, v156, v157
	v_mul_f32_e32 v158, 0x44000000, v61
	v_mul_f32_e32 v159, 0x44000000, v65
	v_med3_f32 v158, v158, s35, v160
	v_med3_f32 v159, v159, s35, v160
	v_cvt_pk_fp8_f32 v155, v158, v159 op_sel:[0,0,1]
	s_nop 0
	ds_write2_b64 v72, v[152:153], v[154:155] offset0:32 offset1:48
	s_waitcnt lgkmcnt(0)
	s_barrier
	ds_read_b128 v[236:239], v75 offset:0
	ds_read_b128 v[240:243], v75 offset:8192
	ds_read_b128 v[244:247], v75 offset:16384
	ds_read_b128 v[248:251], v75 offset:24576
	s_mov_b64 s[68:69], s[52:53]
	s_waitcnt lgkmcnt(3)
	global_store_dwordx4 v76, v[236:239], s[68:69] nt
	s_add_u32 s68, s68, 0x20000
	s_addc_u32 s69, s69, 0
	s_waitcnt lgkmcnt(2)
	global_store_dwordx4 v76, v[240:243], s[68:69] nt
	s_add_u32 s68, s68, 0x20000
	s_addc_u32 s69, s69, 0
	s_waitcnt lgkmcnt(1)
	global_store_dwordx4 v76, v[244:247], s[68:69] nt
	s_add_u32 s68, s68, 0x20000
	s_addc_u32 s69, s69, 0
	s_waitcnt lgkmcnt(0)
	global_store_dwordx4 v76, v[248:251], s[68:69] nt
	s_sub_u32 s41, s41, 1
	s_cmp_eq_u32 s41, 0
	s_cbranch_scc1 .Lcv_done
	s_min_u32 s0, s30, 0x2fff
	s_add_u32 s30, s30, s31
	s_cmp_lt_u32 s0, 0x2000
	s_cbranch_scc0 .Lcv_w2_3
	s_lshr_b32 s1, s0, 8
	s_bfe_u32 s3, s0, 0x40004
	s_and_b32 s0, s0, 15
	s_lshl_b32 s6, s1, 25
	s_lshl_b32 s7, s3, 21
	s_add_u32 s6, s6, s7
	s_lshl_b32 s7, s34, 17
	s_add_u32 s6, s6, s7
	s_lshl_b32 s7, s0, 9
	s_add_u32 s6, s6, s7
	s_add_u32 s62, s8, s6
	s_addc_u32 s63, s9, 0
	s_lshl_b32 s6, s1, 23
	s_lshl_b32 s7, s0, 19
	s_add_u32 s6, s6, s7
	s_lshl_b32 s7, s3, 7
	s_add_u32 s6, s6, s7
	s_add_u32 s52, s12, s6
	s_addc_u32 s53, s13, 0
	s_mov_b32 s70, 0x4000
	s_mov_b32 s71, 0xe4000
	v_mov_b32_e32 v70, v68
	s_branch .Lcv_dec_done_3

.Lcv_dec_done_3:
	global_load_dwordx4 v[2:5], v70, s[62:63] nt
	s_add_u32 s62, s62, s70
	s_addc_u32 s63, s63, 0
	global_load_dwordx4 v[6:9], v70, s[62:63] nt
	s_add_u32 s62, s62, s70
	s_addc_u32 s63, s63, 0
	global_load_dwordx4 v[10:13], v70, s[62:63] nt
	s_add_u32 s62, s62, s70
	s_addc_u32 s63, s63, 0
	global_load_dwordx4 v[14:17], v70, s[62:63] nt
	s_add_u32 s62, s62, s70
	s_addc_u32 s63, s63, 0
	global_load_dwordx4 v[18:21], v70, s[62:63] nt
	s_add_u32 s62, s62, s70
	s_addc_u32 s63, s63, 0
	global_load_dwordx4 v[22:25], v70, s[62:63] nt
	s_add_u32 s62, s62, s70
	s_addc_u32 s63, s63, 0
	global_load_dwordx4 v[26:29], v70, s[62:63] nt
	s_add_u32 s62, s62, s70
	s_addc_u32 s63, s63, 0
	global_load_dwordx4 v[30:33], v70, s[62:63] nt
	s_add_u32 s62, s62, s71
	s_addc_u32 s63, s63, 0
	global_load_dwordx4 v[34:37], v70, s[62:63] nt
	s_add_u32 s62, s62, s70
	s_addc_u32 s63, s63, 0
	global_load_dwordx4 v[38:41], v70, s[62:63] nt
	s_add_u32 s62, s62, s70
	s_addc_u32 s63, s63, 0
	global_load_dwordx4 v[42:45], v70, s[62:63] nt
	s_add_u32 s62, s62, s70
	s_addc_u32 s63, s63, 0
	global_load_dwordx4 v[46:49], v70, s[62:63] nt
	s_add_u32 s62, s62, s70
	s_addc_u32 s63, s63, 0
	global_load_dwordx4 v[50:53], v70, s[62:63] nt
	s_add_u32 s62, s62, s70
	s_addc_u32 s63, s63, 0
	global_load_dwordx4 v[54:57], v70, s[62:63] nt
	s_add_u32 s62, s62, s70
	s_addc_u32 s63, s63, 0
	global_load_dwordx4 v[58:61], v70, s[62:63] nt
	s_add_u32 s62, s62, s70
	s_addc_u32 s63, s63, 0
	global_load_dwordx4 v[62:65], v70, s[62:63] nt
.Lcv_loopB:
	s_waitcnt vmcnt(20)
	v_mul_f32_e32 v156, 0x44000000, v84
	v_mul_f32_e32 v157, 0x44000000, v88
	v_med3_f32 v156, v156, s35, v160
	v_med3_f32 v157, v157, s35, v160
	v_cvt_pk_fp8_f32 v148, v156, v157
	v_mul_f32_e32 v158, 0x44000000, v92
	v_mul_f32_e32 v159, 0x44000000, v96
	v_med3_f32 v158, v158, s35, v160
	v_med3_f32 v159, v159, s35, v160
	v_cvt_pk_fp8_f32 v148, v158, v159 op_sel:[0,0,1]
	v_mul_f32_e32 v156, 0x44000000, v100
	v_mul_f32_e32 v157, 0x44000000, v104
	v_med3_f32 v156, v156, s35, v160
	v_med3_f32 v157, v157, s35, v160
	v_cvt_pk_fp8_f32 v149, v156, v157
	v_mul_f32_e32 v158, 0x44000000, v108
	v_mul_f32_e32 v159, 0x44000000, v112
	v_med3_f32 v158, v158, s35, v160
	v_med3_f32 v159, v159, s35, v160
	v_cvt_pk_fp8_f32 v149, v158, v159 op_sel:[0,0,1]
	v_mul_f32_e32 v156, 0x44000000, v85
	v_mul_f32_e32 v157, 0x44000000, v89
	v_med3_f32 v156, v156, s35, v160
	v_med3_f32 v157, v157, s35, v160
	v_cvt_pk_fp8_f32 v150, v156, v157
	v_mul_f32_e32 v158, 0x44000000, v93
	v_mul_f32_e32 v159, 0x44000000, v97
	v_med3_f32 v158, v158, s35, v160
	v_med3_f32 v159, v159, s35, v160
	v_cvt_pk_fp8_f32 v150, v158, v159 op_sel:[0,0,1]
	v_mul_f32_e32 v156, 0x44000000, v101
	v_mul_f32_e32 v157, 0x44000000, v105
	v_med3_f32 v156, v156, s35, v160
	v_med3_f32 v157, v157, s35, v160
	v_cvt_pk_fp8_f32 v151, v156, v157
	v_mul_f32_e32 v158, 0x44000000, v109
	v_mul_f32_e32 v159, 0x44000000, v113
	v_med3_f32 v158, v158, s35, v160
	v_med3_f32 v159, v159, s35, v160
	v_cvt_pk_fp8_f32 v151, v158, v159 op_sel:[0,0,1]
	v_mul_f32_e32 v156, 0x44000000, v86
	v_mul_f32_e32 v157, 0x44000000, v90
	v_med3_f32 v156, v156, s35, v160
	v_med3_f32 v157, v157, s35, v160
	v_cvt_pk_fp8_f32 v152, v156, v157
	v_mul_f32_e32 v158, 0x44000000, v94
	v_mul_f32_e32 v159, 0x44000000, v98
	v_med3_f32 v158, v158, s35, v160
	v_med3_f32 v159, v159, s35, v160
	v_cvt_pk_fp8_f32 v152, v158, v159 op_sel:[0,0,1]
	ds_write2_b64 v73, v[148:149], v[150:151] offset0:0 offset1:16
	v_mul_f32_e32 v156, 0x44000000, v102
	v_mul_f32_e32 v157, 0x44000000, v106
	v_med3_f32 v156, v156, s35, v160
	v_med3_f32 v157, v157, s35, v160
	v_cvt_pk_fp8_f32 v153, v156, v157
	v_mul_f32_e32 v158, 0x44000000, v110
	v_mul_f32_e32 v159, 0x44000000, v114
	v_med3_f32 v158, v158, s35, v160
	v_med3_f32 v159, v159, s35, v160
	v_cvt_pk_fp8_f32 v153, v158, v159 op_sel:[0,0,1]
	v_mul_f32_e32 v156, 0x44000000, v87
	v_mul_f32_e32 v157, 0x44000000, v91
	v_med3_f32 v156, v156, s35, v160
	v_med3_f32 v157, v157, s35, v160
	v_cvt_pk_fp8_f32 v154, v156, v157
	v_mul_f32_e32 v158, 0x44000000, v95
	v_mul_f32_e32 v159, 0x44000000, v99
	v_med3_f32 v158, v158, s35, v160
	v_med3_f32 v159, v159, s35, v160
	v_cvt_pk_fp8_f32 v154, v158, v159 op_sel:[0,0,1]
	v_mul_f32_e32 v156, 0x44000000, v103
	v_mul_f32_e32 v157, 0x44000000, v107
	v_med3_f32 v156, v156, s35, v160
	v_med3_f32 v157, v157, s35, v160
	v_cvt_pk_fp8_f32 v155, v156, v157
	v_mul_f32_e32 v158, 0x44000000, v111
	v_mul_f32_e32 v159, 0x44000000, v115
	v_med3_f32 v158, v158, s35, v160
	v_med3_f32 v159, v159, s35, v160
	v_cvt_pk_fp8_f32 v155, v158, v159 op_sel:[0,0,1]
	v_mul_f32_e32 v156, 0x44000000, v116
	v_mul_f32_e32 v157, 0x44000000, v120
	v_med3_f32 v156, v156, s35, v160
	v_med3_f32 v157, v157, s35, v160
	v_cvt_pk_fp8_f32 v148, v156, v157
	v_mul_f32_e32 v158, 0x44000000, v124
	v_mul_f32_e32 v159, 0x44000000, v128
	v_med3_f32 v158, v158, s35, v160
	v_med3_f32 v159, v159, s35, v160
	v_cvt_pk_fp8_f32 v148, v158, v159 op_sel:[0,0,1]
	ds_write2_b64 v73, v[152:153], v[154:155] offset0:32 offset1:48
	v_mul_f32_e32 v156, 0x44000000, v132
	v_mul_f32_e32 v157, 0x44000000, v136
	v_med3_f32 v156, v156, s35, v160
	v_med3_f32 v157, v157, s35, v160
	v_cvt_pk_fp8_f32 v149, v156, v157
	v_mul_f32_e32 v158, 0x44000000, v140
	v_mul_f32_e32 v159, 0x44000000, v144
	v_med3_f32 v158, v158, s35, v160
	v_med3_f32 v159, v159, s35, v160
	v_cvt_pk_fp8_f32 v149, v158, v159 op_sel:[0,0,1]
	v_mul_f32_e32 v156, 0x44000000, v117
	v_mul_f32_e32 v157, 0x44000000, v121
	v_med3_f32 v156, v156, s35, v160
	v_med3_f32 v157, v157, s35, v160
	v_cvt_pk_fp8_f32 v150, v156, v157
	v_mul_f32_e32 v158, 0x44000000, v125
	v_mul_f32_e32 v159, 0x44000000, v129
	v_med3_f32 v158, v158, s35, v160
	v_med3_f32 v159, v159, s35, v160
	v_cvt_pk_fp8_f32 v150, v158, v159 op_sel:[0,0,1]
	v_mul_f32_e32 v156, 0x44000000, v133
	v_mul_f32_e32 v157, 0x44000000, v137
	v_med3_f32 v156, v156, s35, v160
	v_med3_f32 v157, v157, s35, v160
	v_cvt_pk_fp8_f32 v151, v156, v157
	v_mul_f32_e32 v158, 0x44000000, v141
	v_mul_f32_e32 v159, 0x44000000, v145
	v_med3_f32 v158, v158, s35, v160
	v_med3_f32 v159, v159, s35, v160
	v_cvt_pk_fp8_f32 v151, v158, v159 op_sel:[0,0,1]
	v_mul_f32_e32 v156, 0x44000000, v118
	v_mul_f32_e32 v157, 0x44000000, v122
	v_med3_f32 v156, v156, s35, v160
	v_med3_f32 v157, v157, s35, v160
	v_cvt_pk_fp8_f32 v152, v156, v157
	v_mul_f32_e32 v158, 0x44000000, v126
	v_mul_f32_e32 v159, 0x44000000, v130
	v_med3_f32 v158, v158, s35, v160
	v_med3_f32 v159, v159, s35, v160
	v_cvt_pk_fp8_f32 v152, v158, v159 op_sel:[0,0,1]
	ds_write2_b64 v74, v[148:149], v[150:151] offset0:0 offset1:16
	v_mul_f32_e32 v156, 0x44000000, v134
	v_mul_f32_e32 v157, 0x44000000, v138
	v_med3_f32 v156, v156, s35, v160
	v_med3_f32 v157, v157, s35, v160
	v_cvt_pk_fp8_f32 v153, v156, v157
	v_mul_f32_e32 v158, 0x44000000, v142
	v_mul_f32_e32 v159, 0x44000000, v146
	v_med3_f32 v158, v158, s35, v160
	v_med3_f32 v159, v159, s35, v160
	v_cvt_pk_fp8_f32 v153, v158, v159 op_sel:[0,0,1]
	v_mul_f32_e32 v156, 0x44000000, v119
	v_mul_f32_e32 v157, 0x44000000, v123
	v_med3_f32 v156, v156, s35, v160
	v_med3_f32 v157, v157, s35, v160
	v_cvt_pk_fp8_f32 v154, v156, v157
	v_mul_f32_e32 v158, 0x44000000, v127
	v_mul_f32_e32 v159, 0x44000000, v131
	v_med3_f32 v158, v158, s35, v160
	v_med3_f32 v159, v159, s35, v160
	v_cvt_pk_fp8_f32 v154, v158, v159 op_sel:[0,0,1]
	v_mul_f32_e32 v156, 0x44000000, v135
	v_mul_f32_e32 v157, 0x44000000, v139
	v_med3_f32 v156, v156, s35, v160
	v_med3_f32 v157, v157, s35, v160
	v_cvt_pk_fp8_f32 v155, v156, v157
	v_mul_f32_e32 v158, 0x44000000, v143
	v_mul_f32_e32 v159, 0x44000000, v147
	v_med3_f32 v158, v158, s35, v160
	v_med3_f32 v159, v159, s35, v160
	v_cvt_pk_fp8_f32 v155, v158, v159 op_sel:[0,0,1]
	s_nop 0
	ds_write2_b64 v74, v[152:153], v[154:155] offset0:32 offset1:48
	s_waitcnt lgkmcnt(0)
	s_barrier
	ds_read_b128 v[236:239], v75 offset:32768
	ds_read_b128 v[240:243], v75 offset:40960
	ds_read_b128 v[244:247], v75 offset:49152
	ds_read_b128 v[248:251], v75 offset:57344
	s_mov_b64 s[68:69], s[58:59]
	s_waitcnt lgkmcnt(3)
	global_store_dwordx4 v76, v[236:239], s[68:69] nt
	s_add_u32 s68, s68, 0x20000
	s_addc_u32 s69, s69, 0
	s_waitcnt lgkmcnt(2)
	global_store_dwordx4 v76, v[240:243], s[68:69] nt
	s_add_u32 s68, s68, 0x20000
	s_addc_u32 s69, s69, 0
	s_waitcnt lgkmcnt(1)
	global_store_dwordx4 v76, v[244:247], s[68:69] nt
	s_add_u32 s68, s68, 0x20000
	s_addc_u32 s69, s69, 0
	s_waitcnt lgkmcnt(0)
	global_store_dwordx4 v76, v[248:251], s[68:69] nt
	s_sub_u32 s41, s41, 1
	s_cmp_eq_u32 s41, 0
	s_cbranch_scc1 .Lcv_done
	s_min_u32 s0, s30, 0x2fff
	s_add_u32 s30, s30, s31
	s_cmp_lt_u32 s0, 0x2000
	s_cbranch_scc0 .Lcv_w2_4
	s_lshr_b32 s1, s0, 8
	s_bfe_u32 s3, s0, 0x40004
	s_and_b32 s0, s0, 15
	s_lshl_b32 s6, s1, 25
	s_lshl_b32 s7, s3, 21
	s_add_u32 s6, s6, s7
	s_lshl_b32 s7, s34, 17
	s_add_u32 s6, s6, s7
	s_lshl_b32 s7, s0, 9
	s_add_u32 s6, s6, s7
	s_add_u32 s62, s8, s6
	s_addc_u32 s63, s9, 0
	s_lshl_b32 s6, s1, 23
	s_lshl_b32 s7, s0, 19
	s_add_u32 s6, s6, s7
	s_lshl_b32 s7, s3, 7
	s_add_u32 s6, s6, s7
	s_add_u32 s58, s12, s6
	s_addc_u32 s59, s13, 0
	s_mov_b32 s70, 0x4000
	s_mov_b32 s71, 0xe4000
	v_mov_b32_e32 v70, v68
	s_branch .Lcv_dec_done_4

.Lcv_dec_done_4:
	global_load_dwordx4 v[84:87], v70, s[62:63] nt
	s_add_u32 s62, s62, s70
	s_addc_u32 s63, s63, 0
	global_load_dwordx4 v[88:91], v70, s[62:63] nt
	s_add_u32 s62, s62, s70
	s_addc_u32 s63, s63, 0
	global_load_dwordx4 v[92:95], v70, s[62:63] nt
	s_add_u32 s62, s62, s70
	s_addc_u32 s63, s63, 0
	global_load_dwordx4 v[96:99], v70, s[62:63] nt
	s_add_u32 s62, s62, s70
	s_addc_u32 s63, s63, 0
	global_load_dwordx4 v[100:103], v70, s[62:63] nt
	s_add_u32 s62, s62, s70
	s_addc_u32 s63, s63, 0
	global_load_dwordx4 v[104:107], v70, s[62:63] nt
	s_add_u32 s62, s62, s70
	s_addc_u32 s63, s63, 0
	global_load_dwordx4 v[108:111], v70, s[62:63] nt
	s_add_u32 s62, s62, s70
	s_addc_u32 s63, s63, 0
	global_load_dwordx4 v[112:115], v70, s[62:63] nt
	s_add_u32 s62, s62, s71
	s_addc_u32 s63, s63, 0
	global_load_dwordx4 v[116:119], v70, s[62:63] nt
	s_add_u32 s62, s62, s70
	s_addc_u32 s63, s63, 0
	global_load_dwordx4 v[120:123], v70, s[62:63] nt
	s_add_u32 s62, s62, s70
	s_addc_u32 s63, s63, 0
	global_load_dwordx4 v[124:127], v70, s[62:63] nt
	s_add_u32 s62, s62, s70
	s_addc_u32 s63, s63, 0
	global_load_dwordx4 v[128:131], v70, s[62:63] nt
	s_add_u32 s62, s62, s70
	s_addc_u32 s63, s63, 0
	global_load_dwordx4 v[132:135], v70, s[62:63] nt
	s_add_u32 s62, s62, s70
	s_addc_u32 s63, s63, 0
	global_load_dwordx4 v[136:139], v70, s[62:63] nt
	s_add_u32 s62, s62, s70
	s_addc_u32 s63, s63, 0
	global_load_dwordx4 v[140:143], v70, s[62:63] nt
	s_add_u32 s62, s62, s70
	s_addc_u32 s63, s63, 0
	global_load_dwordx4 v[144:147], v70, s[62:63] nt
	s_branch .Lcv_loopA
.Lcv_done:
	s_waitcnt vmcnt(0) lgkmcnt(0)
	s_barrier
